# rwkv pass B: the 20 manual wait states before each step's accumulator read cut to 2 (20+ independent instructions already separate the last MFMA from the read)
# baseline (speedup 1.0000x reference)
.LBB0_901:
	v_lshl_add_u64 v[84:85], s[18:19], 0, v[234:235]
	s_mov_b32 s0, 0x58894000
	v_add_co_u32_e32 v86, vcc, s0, v84
	s_mov_b32 s0, 0x58895000
	s_nop 0
	v_addc_co_u32_e32 v87, vcc, 0, v85, vcc
	v_add_co_u32_e32 v84, vcc, s0, v84
	v_lshl_add_u64 v[124:125], s[18:19], 0, v[232:233]
	s_nop 0
	v_addc_co_u32_e32 v85, vcc, 0, v85, vcc
	global_load_dwordx4 v[132:135], v[86:87], off offset:256
	global_load_dwordx4 v[128:131], v[86:87], off offset:1280
	global_load_dwordx4 v[120:123], v[86:87], off offset:2304
	global_load_dwordx4 v[116:119], v[86:87], off offset:3328
	global_load_dwordx4 v[112:115], v[84:85], off offset:256
	global_load_dwordx4 v[108:111], v[84:85], off offset:1280
	global_load_dwordx4 v[88:91], v[84:85], off offset:2304
	s_nop 0
	global_load_dwordx4 v[84:87], v[84:85], off offset:3328
	s_nop 0
	global_load_dwordx4 v[144:147], v[124:125], off offset:-128
	global_load_dwordx4 v[140:143], v[124:125], off offset:-64
	global_load_dwordx4 v[136:139], v[124:125], off
	s_nop 0
	global_load_dwordx4 v[124:127], v[124:125], off offset:64
	s_nop 0
	s_nop 0
	v_lshl_add_u64 v[240:241], s[18:19], 0, v[230:231]
	v_cvt_pk_bf16_f32 v212, v196, v197
	s_mov_b32 s0, 0x60a34000
	v_lshlrev_b32_e32 v213, 16, v212
	v_sub_f32_e32 v196, v196, v213
	v_and_b32_e32 v213, 0xffff0000, v212
	v_sub_f32_e32 v197, v197, v213
	v_cvt_pk_bf16_f32 v196, v196, v197
	v_cvt_pk_bf16_f32 v213, v198, v199
	s_add_i32 s9, s10, 4
	v_lshlrev_b32_e32 v197, 16, v213
	v_sub_f32_e32 v197, v198, v197
	v_and_b32_e32 v198, 0xffff0000, v213
	v_sub_f32_e32 v198, v199, v198
	v_cvt_pk_bf16_f32 v197, v197, v198
	v_cvt_pk_bf16_f32 v214, v204, v205
	s_cmpk_lt_u32 s10, 0x100
	v_lshlrev_b32_e32 v198, 16, v214
	v_and_b32_e32 v199, 0xffff0000, v214
	v_sub_f32_e32 v198, v204, v198
	v_sub_f32_e32 v199, v205, v199
	v_cvt_pk_bf16_f32 v198, v198, v199
	v_cvt_pk_bf16_f32 v215, v206, v207
	v_mov_b32_e32 v237, v83
	v_lshlrev_b32_e32 v199, 16, v215
	v_and_b32_e32 v204, 0xffff0000, v215
	v_sub_f32_e32 v199, v206, v199
	v_sub_f32_e32 v204, v207, v204
	v_cvt_pk_bf16_f32 v199, v199, v204
	v_add_co_u32_e32 v204, vcc, s0, v240
	s_waitcnt vmcnt(37)
	v_mfma_f32_16x16x32_bf16 v[104:107], v[62:65], v[212:215], v[104:107]
	v_addc_co_u32_e32 v205, vcc, 0, v241, vcc
	global_store_dwordx2 v[204:205], v[212:213], off offset:256
	global_store_dwordx2 v[204:205], v[214:215], off offset:288
	v_cvt_pk_bf16_f32 v216, v200, v201
	v_mfma_f32_16x16x32_bf16 v[62:65], v[62:65], v[196:199], v[104:107]
	v_lshlrev_b32_e32 v206, 16, v216
	v_sub_f32_e32 v200, v200, v206
	v_and_b32_e32 v206, 0xffff0000, v216
	v_sub_f32_e32 v201, v201, v206
	v_cvt_pk_bf16_f32 v220, v200, v201
	v_cvt_pk_bf16_f32 v217, v202, v203
	s_cselect_b64 s[0:1], -1, 0
	v_lshlrev_b32_e32 v200, 16, v217
	v_and_b32_e32 v201, 0xffff0000, v217
	v_sub_f32_e32 v200, v202, v200
	v_sub_f32_e32 v201, v203, v201
	v_cvt_pk_bf16_f32 v221, v200, v201
	v_cvt_pk_bf16_f32 v218, v208, v209
	s_and_b64 vcc, s[0:1], exec
	v_lshlrev_b32_e32 v200, 16, v218
	v_and_b32_e32 v201, 0xffff0000, v218
	v_sub_f32_e32 v200, v208, v200
	v_sub_f32_e32 v201, v209, v201
	v_cvt_pk_bf16_f32 v222, v200, v201
	v_cvt_pk_bf16_f32 v219, v210, v211
	s_cselect_b32 s0, s8, 0x40c
	v_mfma_f32_16x16x32_bf16 v[62:65], v[58:61], v[216:219], v[62:65]
	v_lshlrev_b32_e32 v200, 16, v219
	v_and_b32_e32 v201, 0xffff0000, v219
	v_sub_f32_e32 v200, v210, v200
	v_sub_f32_e32 v201, v211, v201
	v_cvt_pk_bf16_f32 v223, v200, v201
	global_store_dwordx2 v[204:205], v[216:217], off offset:320
	global_store_dwordx2 v[204:205], v[218:219], off offset:352
	v_mfma_f32_16x16x32_bf16 v[208:211], v[58:61], v[220:223], v[62:65]
	s_add_u32 s0, s2, s0
	s_addc_u32 s1, s3, 0
	s_lshl_b64 s[0:1], s[0:1], 15
	v_mfma_f32_16x16x32_bf16 v[58:61], v[54:57], v[212:215], v[100:103]
	s_add_u32 s4, s6, s0
	s_addc_u32 s5, s7, s1
	v_mov_b32_e32 v239, v83
	v_mfma_f32_16x16x32_bf16 v[54:57], v[54:57], v[196:199], v[58:61]
	v_lshl_add_u64 v[230:231], v[230:231], 0, s[14:15]
	v_lshl_add_u64 v[232:233], v[232:233], 0, s[16:17]
	v_lshl_add_u64 v[234:235], v[234:235], 0, s[16:17]
	v_mfma_f32_16x16x32_bf16 v[54:57], v[50:53], v[216:219], v[54:57]
	v_mfma_f32_16x16x32_bf16 v[204:207], v[50:53], v[220:223], v[54:57]
	v_mfma_f32_16x16x32_bf16 v[50:53], v[78:81], v[212:215], v[96:99]
	v_mfma_f32_16x16x32_bf16 v[50:53], v[78:81], v[196:199], v[50:53]
	v_mfma_f32_16x16x32_bf16 v[50:53], v[74:77], v[216:219], v[50:53]
	v_mfma_f32_16x16x32_bf16 v[200:203], v[74:77], v[220:223], v[50:53]
	s_waitcnt vmcnt(40)
	v_mfma_f32_16x16x32_bf16 v[50:53], v[70:73], v[212:215], v[92:95]
	v_mfma_f32_16x16x32_bf16 v[50:53], v[70:73], v[196:199], v[50:53]
	s_nop 1
	v_lshl_add_u64 v[92:93], s[4:5], 0, v[236:237]
	v_lshl_add_u64 v[92:93], v[92:93], 0, v[238:239]
	v_lshl_add_u64 v[94:95], v[92:93], 0, s[12:13]
	v_mfma_f32_16x16x32_bf16 v[50:53], v[66:69], v[216:219], v[50:53]
	v_mfma_f32_16x16x32_bf16 v[196:199], v[66:69], v[220:223], v[50:53]
	v_lshl_add_u64 v[66:67], s[4:5], 0, v[82:83]
	v_add_co_u32_e64 v66, s[0:1], s62, v66
	global_load_dwordx4 v[62:65], v82, s[4:5]
	global_load_dwordx4 v[58:61], v82, s[4:5] offset:1024
	global_load_dwordx4 v[54:57], v82, s[4:5] offset:2048
	s_nop 1
	global_load_dwordx4 v[50:53], v82, s[4:5] offset:3072
	v_addc_co_u32_e64 v67, s[0:1], 0, v67, s[0:1]
	v_add_co_u32_e64 v92, s[0:1], s69, v92
	global_load_dwordx4 v[78:81], v[66:67], off
	global_load_dwordx4 v[74:77], v[66:67], off offset:1024
	global_load_dwordx4 v[70:73], v[66:67], off offset:2048
	s_nop 0
	global_load_dwordx4 v[66:69], v[66:67], off offset:3072
	v_addc_co_u32_e64 v93, s[0:1], 0, v93, s[0:1]
	global_load_dwordx4 v[104:107], v[92:93], off
	global_load_dwordx4 v[100:103], v[94:95], off offset:64
	global_load_dwordx4 v[96:99], v[94:95], off offset:128
	s_nop 0
	global_load_dwordx4 v[92:95], v[94:95], off offset:192
	s_nop 0
	s_nop 0
	s_mov_b32 s0, 0x60a44000
	v_cvt_pk_bf16_f32 v212, v208, v209
	v_add_co_u32_e64 v220, s[0:1], s0, v240
	v_lshlrev_b32_e32 v213, 16, v212
	v_sub_f32_e32 v208, v208, v213
	v_and_b32_e32 v213, 0xffff0000, v212
	v_sub_f32_e32 v209, v209, v213
	v_cvt_pk_bf16_f32 v208, v208, v209
	v_cvt_pk_bf16_f32 v213, v210, v211
	v_addc_co_u32_e64 v221, s[0:1], 0, v241, s[0:1]
	v_lshlrev_b32_e32 v209, 16, v213
	v_sub_f32_e32 v209, v210, v209
	v_and_b32_e32 v210, 0xffff0000, v213
	v_sub_f32_e32 v210, v211, v210
	v_cvt_pk_bf16_f32 v209, v209, v210
	v_cvt_pk_bf16_f32 v214, v204, v205
	s_min_u32 s0, s10, 0xfe
	v_lshlrev_b32_e32 v210, 16, v214
	v_sub_f32_e32 v204, v204, v210
	v_and_b32_e32 v210, 0xffff0000, v214
	v_sub_f32_e32 v205, v205, v210
	v_cvt_pk_bf16_f32 v210, v204, v205
	v_cvt_pk_bf16_f32 v215, v206, v207
	s_lshl_b32 s0, s0, 2
	v_lshlrev_b32_e32 v204, 16, v215
	v_and_b32_e32 v205, 0xffff0000, v215
	s_waitcnt vmcnt(39)
	v_mfma_f32_16x16x32_bf16 v[46:49], v[10:13], v[212:215], v[46:49]
	v_sub_f32_e32 v204, v206, v204
	v_sub_f32_e32 v205, v207, v205
	v_cvt_pk_bf16_f32 v211, v204, v205
	global_store_dwordx2 v[220:221], v[212:213], off offset:256
	global_store_dwordx2 v[220:221], v[214:215], off offset:288
	v_cvt_pk_bf16_f32 v204, v200, v201
	v_mfma_f32_16x16x32_bf16 v[10:13], v[10:13], v[208:211], v[46:49]
	v_lshlrev_b32_e32 v205, 16, v204
	v_sub_f32_e32 v200, v200, v205
	v_and_b32_e32 v205, 0xffff0000, v204
	v_sub_f32_e32 v201, v201, v205
	v_cvt_pk_bf16_f32 v216, v200, v201
	v_cvt_pk_bf16_f32 v205, v202, v203
	s_add_i32 s0, s0, 20
	v_lshlrev_b32_e32 v200, 16, v205
	v_sub_f32_e32 v200, v202, v200
	v_and_b32_e32 v201, 0xffff0000, v205
	v_sub_f32_e32 v201, v203, v201
	v_cvt_pk_bf16_f32 v217, v200, v201
	v_cvt_pk_bf16_f32 v206, v196, v197
	s_add_u32 s0, s2, s0
	v_lshlrev_b32_e32 v200, 16, v206
	v_sub_f32_e32 v196, v196, v200
	v_and_b32_e32 v200, 0xffff0000, v206
	v_sub_f32_e32 v197, v197, v200
	v_cvt_pk_bf16_f32 v218, v196, v197
	v_cvt_pk_bf16_f32 v207, v198, v199
	s_addc_u32 s1, s3, 0
	v_mfma_f32_16x16x32_bf16 v[10:13], v[2:5], v[204:207], v[10:13]
	v_lshlrev_b32_e32 v196, 16, v207
	v_and_b32_e32 v197, 0xffff0000, v207
	v_sub_f32_e32 v196, v198, v196
	v_sub_f32_e32 v197, v199, v197
	v_cvt_pk_bf16_f32 v219, v196, v197
	global_store_dwordx2 v[220:221], v[204:205], off offset:320
	global_store_dwordx2 v[220:221], v[206:207], off offset:352
	v_mfma_f32_16x16x32_bf16 v[220:223], v[2:5], v[216:219], v[10:13]
	s_lshl_b64 s[0:1], s[0:1], 15
	s_add_u32 s4, s6, s0
	s_addc_u32 s5, s7, s1
	v_mfma_f32_16x16x32_bf16 v[2:5], v[6:9], v[212:215], v[42:45]
	v_mfma_f32_16x16x32_bf16 v[2:5], v[6:9], v[208:211], v[2:5]
	v_mfma_f32_16x16x32_bf16 v[2:5], v[26:29], v[204:207], v[2:5]
	v_mfma_f32_16x16x32_bf16 v[246:249], v[26:29], v[216:219], v[2:5]
	v_mfma_f32_16x16x32_bf16 v[2:5], v[14:17], v[212:215], v[38:41]
	v_mfma_f32_16x16x32_bf16 v[2:5], v[14:17], v[208:211], v[2:5]
	v_lshl_add_u64 v[14:15], s[4:5], 0, v[82:83]
	v_mfma_f32_16x16x32_bf16 v[2:5], v[18:21], v[204:207], v[2:5]
	v_mfma_f32_16x16x32_bf16 v[200:203], v[18:21], v[216:219], v[2:5]
	v_mfma_f32_16x16x32_bf16 v[2:5], v[22:25], v[212:215], v[34:37]
	v_mfma_f32_16x16x32_bf16 v[2:5], v[22:25], v[208:211], v[2:5]
	s_nop 1
	v_lshl_add_u64 v[34:35], s[4:5], 0, v[236:237]
	v_lshl_add_u64 v[34:35], v[34:35], 0, v[238:239]
	v_lshl_add_u64 v[36:37], v[34:35], 0, s[12:13]
	v_mfma_f32_16x16x32_bf16 v[2:5], v[30:33], v[204:207], v[2:5]
	v_mfma_f32_16x16x32_bf16 v[196:199], v[30:33], v[216:219], v[2:5]
	v_add_co_u32_e64 v30, s[0:1], s62, v14
	global_load_dwordx4 v[10:13], v82, s[4:5]
	s_nop 4
	global_load_dwordx4 v[2:5], v82, s[4:5] offset:1024
	global_load_dwordx4 v[6:9], v82, s[4:5] offset:2048
	global_load_dwordx4 v[26:29], v82, s[4:5] offset:3072
	v_addc_co_u32_e64 v31, s[0:1], 0, v15, s[0:1]
	v_add_co_u32_e64 v34, s[0:1], s69, v34
	global_load_dwordx4 v[14:17], v[30:31], off
	global_load_dwordx4 v[18:21], v[30:31], off offset:1024
	global_load_dwordx4 v[22:25], v[30:31], off offset:2048
	s_nop 0
	global_load_dwordx4 v[30:33], v[30:31], off offset:3072
	v_addc_co_u32_e64 v35, s[0:1], 0, v35, s[0:1]
	global_load_dwordx4 v[46:49], v[34:35], off
	global_load_dwordx4 v[42:45], v[36:37], off offset:64
	global_load_dwordx4 v[38:41], v[36:37], off offset:128
	s_nop 0
	global_load_dwordx4 v[34:37], v[36:37], off offset:192
	s_nop 0
	s_nop 0
	s_mov_b32 s0, 0x60a54000
	v_cvt_pk_bf16_f32 v212, v220, v221
	s_nop 0
	v_lshlrev_b32_e32 v204, 16, v212
	v_sub_f32_e32 v204, v220, v204
	v_and_b32_e32 v205, 0xffff0000, v212
	v_sub_f32_e32 v205, v221, v205
	v_cvt_pk_bf16_f32 v216, v204, v205
	v_cvt_pk_bf16_f32 v213, v222, v223
	s_nop 0
	v_lshlrev_b32_e32 v204, 16, v213
	v_sub_f32_e32 v204, v222, v204
	v_and_b32_e32 v205, 0xffff0000, v213
	v_sub_f32_e32 v205, v223, v205
	v_cvt_pk_bf16_f32 v217, v204, v205
	v_cvt_pk_bf16_f32 v214, v246, v247
	s_nop 0
	v_lshlrev_b32_e32 v204, 16, v214
	v_sub_f32_e32 v204, v246, v204
	v_and_b32_e32 v205, 0xffff0000, v214
	v_sub_f32_e32 v205, v247, v205
	v_cvt_pk_bf16_f32 v218, v204, v205
	v_cvt_pk_bf16_f32 v215, v248, v249
	s_nop 0
	v_lshlrev_b32_e32 v204, 16, v215
	v_sub_f32_e32 v204, v248, v204
	v_and_b32_e32 v205, 0xffff0000, v215
	v_sub_f32_e32 v205, v249, v205
	v_cvt_pk_bf16_f32 v219, v204, v205
	v_add_co_u32_e64 v204, s[0:1], s0, v240
	s_waitcnt vmcnt(45)
	v_mfma_f32_16x16x32_bf16 v[180:183], v[148:151], v[212:215], v[180:183]
	v_addc_co_u32_e64 v205, s[0:1], 0, v241, s[0:1]
	global_store_dwordx2 v[204:205], v[212:213], off offset:256
	global_store_dwordx2 v[204:205], v[214:215], off offset:288
	v_cvt_pk_bf16_f32 v220, v200, v201
	v_mfma_f32_16x16x32_bf16 v[148:151], v[148:151], v[216:219], v[180:183]
	v_lshlrev_b32_e32 v206, 16, v220
	v_sub_f32_e32 v200, v200, v206
	v_and_b32_e32 v206, 0xffff0000, v220
	v_sub_f32_e32 v201, v201, v206
	v_cvt_pk_bf16_f32 v246, v200, v201
	v_cvt_pk_bf16_f32 v221, v202, v203
	s_min_u32 s0, s10, 0xfd
	v_lshlrev_b32_e32 v200, 16, v221
	v_sub_f32_e32 v200, v202, v200
	v_and_b32_e32 v201, 0xffff0000, v221
	v_sub_f32_e32 v201, v203, v201
	v_cvt_pk_bf16_f32 v247, v200, v201
	v_cvt_pk_bf16_f32 v222, v196, v197
	s_lshl_b32 s0, s0, 2
	v_lshlrev_b32_e32 v200, 16, v222
	v_sub_f32_e32 v196, v196, v200
	v_and_b32_e32 v200, 0xffff0000, v222
	v_sub_f32_e32 v197, v197, v200
	v_cvt_pk_bf16_f32 v248, v196, v197
	v_cvt_pk_bf16_f32 v223, v198, v199
	s_add_i32 s0, s0, 24
	v_mfma_f32_16x16x32_bf16 v[148:151], v[152:155], v[220:223], v[148:151]
	v_lshlrev_b32_e32 v196, 16, v223
	v_and_b32_e32 v197, 0xffff0000, v223
	v_sub_f32_e32 v196, v198, v196
	v_sub_f32_e32 v197, v199, v197
	v_cvt_pk_bf16_f32 v249, v196, v197
	global_store_dwordx2 v[204:205], v[220:221], off offset:320
	global_store_dwordx2 v[204:205], v[222:223], off offset:352
	v_mfma_f32_16x16x32_bf16 v[208:211], v[152:155], v[246:249], v[148:151]
	s_add_u32 s0, s2, s0
	s_addc_u32 s1, s3, 0
	s_lshl_b64 s[0:1], s[0:1], 15
	v_mfma_f32_16x16x32_bf16 v[148:151], v[156:159], v[212:215], v[184:187]
	s_add_u32 s4, s6, s0
	s_addc_u32 s5, s7, s1
	v_lshl_add_u64 v[180:181], s[4:5], 0, v[236:237]
	v_mfma_f32_16x16x32_bf16 v[148:151], v[156:159], v[216:219], v[148:151]
	v_lshl_add_u64 v[180:181], v[180:181], 0, v[238:239]
	s_add_i32 s8, s8, 16
	s_mov_b32 s10, s9
	v_mfma_f32_16x16x32_bf16 v[148:151], v[160:163], v[220:223], v[148:151]
	v_mfma_f32_16x16x32_bf16 v[204:207], v[160:163], v[246:249], v[148:151]
	v_mfma_f32_16x16x32_bf16 v[148:151], v[164:167], v[212:215], v[188:191]
	v_mfma_f32_16x16x32_bf16 v[148:151], v[164:167], v[216:219], v[148:151]
	v_lshl_add_u64 v[164:165], s[4:5], 0, v[82:83]
	v_mfma_f32_16x16x32_bf16 v[148:151], v[168:171], v[220:223], v[148:151]
	v_mfma_f32_16x16x32_bf16 v[200:203], v[168:171], v[246:249], v[148:151]
	s_waitcnt vmcnt(48)
	v_mfma_f32_16x16x32_bf16 v[148:151], v[172:175], v[212:215], v[192:195]
	v_mfma_f32_16x16x32_bf16 v[148:151], v[172:175], v[216:219], v[148:151]
	s_nop 1
	v_lshl_add_u64 v[192:193], v[180:181], 0, s[12:13]
	v_mfma_f32_16x16x32_bf16 v[148:151], v[176:179], v[220:223], v[148:151]
	v_mfma_f32_16x16x32_bf16 v[196:199], v[176:179], v[246:249], v[148:151]
	v_add_co_u32_e64 v176, s[0:1], s62, v164
	s_nop 5
	global_load_dwordx4 v[148:151], v82, s[4:5]
	global_load_dwordx4 v[152:155], v82, s[4:5] offset:1024
	global_load_dwordx4 v[156:159], v82, s[4:5] offset:2048
	global_load_dwordx4 v[160:163], v82, s[4:5] offset:3072
	v_addc_co_u32_e64 v177, s[0:1], 0, v165, s[0:1]
	v_add_co_u32_e64 v180, s[0:1], s69, v180
	global_load_dwordx4 v[164:167], v[176:177], off
	global_load_dwordx4 v[168:171], v[176:177], off offset:1024
	global_load_dwordx4 v[172:175], v[176:177], off offset:2048
	s_nop 0
	global_load_dwordx4 v[176:179], v[176:177], off offset:3072
	v_addc_co_u32_e64 v181, s[0:1], 0, v181, s[0:1]
	global_load_dwordx4 v[180:183], v[180:181], off
	s_nop 0
	global_load_dwordx4 v[184:187], v[192:193], off offset:64
	global_load_dwordx4 v[188:191], v[192:193], off offset:128
	s_nop 0
	global_load_dwordx4 v[192:195], v[192:193], off offset:192
	s_nop 0
	s_nop 0
	s_mov_b32 s0, 0x60a64000
	v_cvt_pk_bf16_f32 v220, v208, v209
	s_nop 0
	v_lshlrev_b32_e32 v212, 16, v220
	v_sub_f32_e32 v208, v208, v212
	v_and_b32_e32 v212, 0xffff0000, v220
	v_sub_f32_e32 v209, v209, v212
	v_cvt_pk_bf16_f32 v216, v208, v209
	v_cvt_pk_bf16_f32 v221, v210, v211
	s_nop 0
	v_lshlrev_b32_e32 v208, 16, v221
	v_sub_f32_e32 v208, v210, v208
	v_and_b32_e32 v209, 0xffff0000, v221
	v_sub_f32_e32 v209, v211, v209
	v_cvt_pk_bf16_f32 v217, v208, v209
	v_cvt_pk_bf16_f32 v222, v204, v205
	s_nop 0
	v_lshlrev_b32_e32 v208, 16, v222
	v_sub_f32_e32 v204, v204, v208
	v_and_b32_e32 v208, 0xffff0000, v222
	v_sub_f32_e32 v205, v205, v208
	v_cvt_pk_bf16_f32 v218, v204, v205
	v_cvt_pk_bf16_f32 v223, v206, v207
	s_nop 0
	v_lshlrev_b32_e32 v204, 16, v223
	v_sub_f32_e32 v204, v206, v204
	v_and_b32_e32 v205, 0xffff0000, v223
	v_sub_f32_e32 v205, v207, v205
	v_cvt_pk_bf16_f32 v219, v204, v205
	v_add_co_u32_e64 v204, s[0:1], s0, v240
	s_waitcnt vmcnt(51)
	v_mfma_f32_16x16x32_bf16 v[144:147], v[132:135], v[220:223], v[144:147]
	v_addc_co_u32_e64 v205, s[0:1], 0, v241, s[0:1]
	global_store_dwordx2 v[204:205], v[220:221], off offset:256
	global_store_dwordx2 v[204:205], v[222:223], off offset:288
	v_cvt_pk_bf16_f32 v208, v200, v201
	v_mfma_f32_16x16x32_bf16 v[132:135], v[132:135], v[216:219], v[144:147]
	v_lshlrev_b32_e32 v206, 16, v208
	v_sub_f32_e32 v200, v200, v206
	v_and_b32_e32 v206, 0xffff0000, v208
	v_sub_f32_e32 v201, v201, v206
	v_cvt_pk_bf16_f32 v212, v200, v201
	v_cvt_pk_bf16_f32 v209, v202, v203
	s_nop 0
	v_lshlrev_b32_e32 v200, 16, v209
	v_sub_f32_e32 v200, v202, v200
	v_and_b32_e32 v201, 0xffff0000, v209
	v_sub_f32_e32 v201, v203, v201
	v_cvt_pk_bf16_f32 v213, v200, v201
	v_cvt_pk_bf16_f32 v210, v196, v197
	s_nop 0
	v_lshlrev_b32_e32 v200, 16, v210
	v_sub_f32_e32 v196, v196, v200
	v_and_b32_e32 v200, 0xffff0000, v210
	v_sub_f32_e32 v197, v197, v200
	v_cvt_pk_bf16_f32 v214, v196, v197
	v_cvt_pk_bf16_f32 v211, v198, v199
	s_nop 0
	v_mfma_f32_16x16x32_bf16 v[132:135], v[128:131], v[208:211], v[132:135]
	v_lshlrev_b32_e32 v196, 16, v211
	v_and_b32_e32 v197, 0xffff0000, v211
	v_sub_f32_e32 v196, v198, v196
	v_sub_f32_e32 v197, v199, v197
	v_cvt_pk_bf16_f32 v215, v196, v197
	global_store_dwordx2 v[204:205], v[208:209], off offset:320
	global_store_dwordx2 v[204:205], v[210:211], off offset:352
	v_mfma_f32_16x16x32_bf16 v[196:199], v[128:131], v[212:215], v[132:135]
	s_waitcnt vmcnt(54)
	v_mfma_f32_16x16x32_bf16 v[128:131], v[120:123], v[220:223], v[140:143]
	v_mfma_f32_16x16x32_bf16 v[120:123], v[120:123], v[216:219], v[128:131]
	v_mfma_f32_16x16x32_bf16 v[120:123], v[116:119], v[208:211], v[120:123]
	v_mfma_f32_16x16x32_bf16 v[204:207], v[116:119], v[212:215], v[120:123]
	s_waitcnt vmcnt(53)
	v_mfma_f32_16x16x32_bf16 v[116:119], v[112:115], v[220:223], v[136:139]
	v_mfma_f32_16x16x32_bf16 v[112:115], v[112:115], v[216:219], v[116:119]
	v_mfma_f32_16x16x32_bf16 v[112:115], v[108:111], v[208:211], v[112:115]
	v_mfma_f32_16x16x32_bf16 v[200:203], v[108:111], v[212:215], v[112:115]
	s_waitcnt vmcnt(52)
	v_mfma_f32_16x16x32_bf16 v[108:111], v[88:91], v[220:223], v[124:127]
	v_mfma_f32_16x16x32_bf16 v[88:91], v[88:91], v[216:219], v[108:111]
	v_mfma_f32_16x16x32_bf16 v[88:91], v[84:87], v[208:211], v[88:91]
	v_mfma_f32_16x16x32_bf16 v[208:211], v[84:87], v[212:215], v[88:91]
	s_cbranch_vccnz .LBB0_901
	s_waitcnt vmcnt(30)
	v_mov_b32_e32 v2, v0
	s_waitcnt vmcnt(0)
	buffer_wbl2 sc1
	s_waitcnt vmcnt(0)
	s_waitcnt vmcnt(0)
	s_nop 0
	v_and_b32_e32 v2, 63, v2
	v_cmp_eq_u32_e32 vcc, 0, v2
	s_and_saveexec_b64 s[0:1], vcc
	s_cbranch_execz .LBB0_905
	s_mov_b64 s[2:3], exec
	v_mbcnt_lo_u32_b32 v2, s2, 0
	v_mbcnt_hi_u32_b32 v2, s3, v2
	v_cmp_eq_u32_e32 vcc, 0, v2
	s_and_b64 s[4:5], exec, vcc
	s_mov_b64 exec, s[4:5]
	s_cbranch_execz .LBB0_905
	s_bcnt1_i32_b64 s2, s[2:3]
	v_mov_b32_e32 v2, s2
	v_readlane_b32 s2, v253, 15
	v_readlane_b32 s3, v253, 16
	s_nop 4
	global_atomic_add v83, v2, s[2:3]
